# v59 + GEMM prologues issue K-tile 1 loads before the first wait + router queue-counter read not waited at phase start
# baseline (speedup 1.0000x reference)
.LBB0_99:
	s_add_i32 s4, 0, 0x21000
	s_add_u32 s38, s90, 0x2800000
	s_addc_u32 s39, s91, 0
	s_add_u32 s12, s90, 0x300000
	s_addc_u32 s13, s91, 0
	s_add_u32 s14, s90, 0x340000
	v_readlane_b32 s17, v255, 25
	s_addc_u32 s15, s91, 0
	s_bfe_u32 s1, s17, 0x20006
	s_lshl_b32 s40, s0, 6
	s_lshl_b32 s5, s0, 13
	s_lshl_b32 s41, s1, 5
	s_lshl_b32 s16, s1, 12
	s_add_u32 s0, s22, 0x80
	s_addc_u32 s1, s23, 0
	s_nop 0
	s_nop 0
	s_add_i32 m0, s33, 0x18000
	v_lshl_add_u64 v[2:3], s[0:1], 0, v[192:193]
	global_load_lds_dwordx4 v[2:3], off
	s_add_i32 m0, s33, 0x1a000
	v_lshl_add_u64 v[2:3], s[0:1], 0, v[194:195]
	s_add_u32 s0, s90, 0x800080
	s_addc_u32 s1, s91, 0
	s_add_i32 s42, s33, 0x8000
	global_load_lds_dwordx4 v[2:3], off
	s_mov_b32 m0, s42
	v_lshl_add_u64 v[2:3], s[0:1], 0, v[64:65]
	s_add_i32 s43, s33, 0xa000
	global_load_lds_dwordx4 v[2:3], off
	v_lshl_add_u64 v[2:3], s[0:1], 0, v[136:137]
	s_add_u32 s0, s22, 0x80080
	s_mov_b32 m0, s43
	s_addc_u32 s1, s23, 0
	global_load_lds_dwordx4 v[2:3], off
	s_add_i32 m0, s33, 0x1c000
	v_lshl_add_u64 v[2:3], s[0:1], 0, v[192:193]
	global_load_lds_dwordx4 v[2:3], off
	v_lshl_add_u64 v[2:3], s[0:1], 0, v[194:195]
	s_add_i32 m0, s33, 0x1e000
	v_lshl_add_u32 v195, v0, 4, s4
	global_load_lds_dwordx4 v[2:3], off
	v_and_b32_e32 v1, 48, v0
	v_lshlrev_b32_e32 v2, 6, v0
	s_movk_i32 s0, 0x3c0
	v_lshlrev_b32_e32 v0, 2, v0
	v_and_or_b32 v1, v2, s0, v1
	v_and_b32_e32 v0, 32, v0
	s_waitcnt vmcnt(8)
	s_barrier
	s_waitcnt vmcnt(6)
	s_cmpk_lt_u32 s17, 0x100
	v_bitop3_b32 v2, v1, s5, v0 bitop3:0xde
	v_bitop3_b32 v203, v1, s16, v0 bitop3:0xde
	s_cselect_b64 s[16:17], -1, 0
	s_lshl_b32 s0, s94, 2
	s_and_b32 s44, s0, 4
	s_add_i32 s45, 0, 0x10000
	s_add_i32 s46, 0, 0x14000
	v_add_u32_e32 v204, 0, v2
	v_mov_b32_e32 v205, 0x3e38aa3b
	v_mov_b32_e32 v206, v192
	s_barrier
	s_branch .LBB0_102

.LBB0_488:
	s_add_i32 s12, 0, 0x21000
	s_add_u32 s8, s90, 0xe800000
	s_addc_u32 s9, s91, 0
	s_lshl_b32 s10, s94, 5
	s_and_b32 s34, s10, 0x60
	s_lshl_b32 s33, s1, 6
	s_lshl_b32 s1, s1, 13
	s_lshl_b32 s13, s34, 7
	s_add_u32 s10, s18, 0x80
	s_addc_u32 s11, s19, 0
	s_nop 0
	s_nop 0
	s_add_i32 m0, s27, 0x18000
	v_lshl_add_u64 v[2:3], s[10:11], 0, v[136:137]
	global_load_lds_dwordx4 v[2:3], off
	s_add_i32 m0, s27, 0x1a000
	v_lshl_add_u64 v[2:3], s[10:11], 0, v[138:139]
	s_add_u32 s10, s90, 0xc800080
	s_addc_u32 s11, s91, 0
	s_add_i32 s35, s27, 0x8000
	global_load_lds_dwordx4 v[2:3], off
	s_mov_b32 m0, s35
	v_lshl_add_u64 v[2:3], s[10:11], 0, v[8:9]
	s_add_i32 s36, s27, 0xa000
	global_load_lds_dwordx4 v[2:3], off
	v_lshl_add_u64 v[2:3], s[10:11], 0, v[140:141]
	s_add_u32 s10, s18, 0x80080
	s_mov_b32 m0, s36
	s_addc_u32 s11, s19, 0
	global_load_lds_dwordx4 v[2:3], off
	s_add_i32 m0, s27, 0x1c000
	v_lshl_add_u64 v[2:3], s[10:11], 0, v[136:137]
	global_load_lds_dwordx4 v[2:3], off
	v_lshl_add_u64 v[2:3], s[10:11], 0, v[138:139]
	s_add_i32 m0, s27, 0x1e000
	s_sext_i32_i8 s42, s0
	global_load_lds_dwordx4 v[2:3], off
	v_lshl_add_u32 v137, v0, 4, s12
	v_and_b32_e32 v1, 48, v0
	v_lshlrev_b32_e32 v2, 6, v0
	s_movk_i32 s0, 0x3c0
	v_lshlrev_b32_e32 v0, 2, v0
	v_and_or_b32 v1, v2, s0, v1
	v_and_b32_e32 v0, 32, v0
	s_waitcnt vmcnt(8)
	s_barrier
	s_waitcnt vmcnt(6)
	v_readlane_b32 s0, v255, 25
	v_bitop3_b32 v2, v1, s1, v0 bitop3:0xde
	s_cmpk_lt_u32 s0, 0x100
	v_bitop3_b32 v139, v1, s13, v0 bitop3:0xde
	s_cselect_b64 s[10:11], -1, 0
	s_add_i32 s37, 0, 0x10000
	s_add_i32 s38, 0, 0x14000
	v_add_u32_e32 v147, 0, v2
	s_barrier
	s_branch .LBB0_491

.LBB0_562:
	v_writelane_b32 v255, s72, 31
	s_cmp_gt_i32 s14, 5
	s_cselect_b64 s[0:1], -1, 0
	v_writelane_b32 v255, s73, 32
	v_writelane_b32 v255, s74, 33
	v_writelane_b32 v255, s75, 34
	v_writelane_b32 v255, s76, 35
	v_writelane_b32 v255, s77, 36
	v_writelane_b32 v255, s78, 37
	v_writelane_b32 v255, s79, 38
	v_writelane_b32 v255, s80, 39
	v_writelane_b32 v255, s81, 40
	v_writelane_b32 v255, s82, 41
	v_writelane_b32 v255, s83, 42
	s_cmp_lt_i32 s15, 6
	v_writelane_b32 v255, s84, 43
	s_cselect_b64 s[2:3], -1, 0
	v_writelane_b32 v255, s85, 44
	s_or_b64 s[0:1], s[0:1], s[2:3]
	v_writelane_b32 v255, s86, 45
	s_and_b64 vcc, exec, s[0:1]
	v_writelane_b32 v255, s87, 46
	s_cbranch_vccnz .LBB0_654
	s_waitcnt vmcnt(11)
	v_mbcnt_lo_u32_b32 v0, -1, 0
	v_mbcnt_hi_u32_b32 v0, -1, v0
	v_readlane_b32 s0, v255, 4
	v_mov_b32_e32 v56, 1
	s_nop 0
	v_add_u32_e32 v0, s0, v0
	s_nop 0
	v_cmp_eq_u32_e32 vcc, 0, v0
	s_and_saveexec_b64 s[0:1], vcc
	s_cbranch_execz .LBB0_565
	v_mov_b32_e32 v0, 0
	global_load_dword v56, v0, s[90:91] offset:1024 sc1
	s_movk_i32 s2, 0x900

.LBB0_589:
	v_mbcnt_lo_u32_b32 v0, -1, 0
	v_mbcnt_hi_u32_b32 v0, -1, v0
	v_readlane_b32 s0, v255, 4
	s_nop 1
	v_add_u32_e32 v0, s0, v0
	s_nop 0
	v_cmp_eq_u32_e32 vcc, 0, v0
	s_and_saveexec_b64 s[0:1], vcc
	s_add_i32 s2, 0, 0x20800
	v_mov_b32_e32 v0, s2
	s_waitcnt vmcnt(0)
	v_cmp_gt_u32_e32 vcc, 0x900, v56
	s_nop 1
	v_cndmask_b32_e64 v56, 0, 1, vcc
	ds_write_b32 v0, v56
	s_or_b64 exec, exec, s[0:1]
	s_add_i32 s0, 0, 0x20800
	v_mov_b32_e32 v0, s0
	s_waitcnt lgkmcnt(0)
	s_barrier
	ds_read_b32 v0, v0
	s_waitcnt lgkmcnt(0)
	s_barrier
	v_readfirstlane_b32 s0, v0
	s_cmp_eq_u32 s0, 0
	s_cbranch_scc1 .LBB0_601
	s_add_u32 s2, s90, 0x2a800000
	s_addc_u32 s3, s91, 0
	s_add_u32 s14, s90, 0x4a800000
	v_readlane_b32 s6, v255, 25
	s_addc_u32 s15, s91, 0
	s_lshr_b32 s16, s6, 8
	v_readlane_b32 s0, v255, 4
	s_lshl_b32 s7, s16, 3
	v_mbcnt_lo_u32_b32 v0, -1, 0
	v_mbcnt_hi_u32_b32 v0, -1, v0
	s_or_b32 s8, s7, 1
	v_add_u32_e32 v1, s0, v0
	s_lshl_b32 s6, s94, 8
	s_waitcnt vmcnt(6)
	v_bitop3_b32 v21, v1, s8, 15 bitop3:0x6c
	s_or_b32 s8, s7, 2
	v_bitop3_b32 v22, v1, s8, 15 bitop3:0x6c
	s_or_b32 s8, s7, 3
	v_bitop3_b32 v23, v1, s8, 15 bitop3:0x6c
	s_or_b32 s8, s7, 4
	v_lshlrev_b32_e32 v0, 2, v1
	s_waitcnt vmcnt(5)
	v_bitop3_b32 v24, v1, s8, 15 bitop3:0x6c
	s_or_b32 s8, s7, 5
	v_and_b32_e32 v0, 0xfc, v0
	v_lshlrev_b32_e32 v2, 4, v1
	s_movk_i32 s4, 0x70
	v_lshrrev_b32_e32 v3, 2, v1
	v_add_u32_e32 v4, 0x200, v1
	v_add_u32_e32 v5, 0x400, v1
	v_add_u32_e32 v6, 0x600, v1
	v_add_u32_e32 v7, 0x800, v1
	v_add_u32_e32 v8, 0xa00, v1
	v_add_u32_e32 v9, 0xc00, v1
	v_add_u32_e32 v10, 0xe00, v1
	v_add_u32_e32 v11, 0x1000, v1
	v_add_u32_e32 v12, 0x1200, v1
	v_add_u32_e32 v13, 0x1400, v1
	v_add_u32_e32 v14, 0x1600, v1
	v_add_u32_e32 v15, 0x1800, v1
	v_add_u32_e32 v16, 0x1a00, v1
	v_add_u32_e32 v17, 0x1c00, v1
	v_add_u32_e32 v18, 0x1e00, v1
	s_and_b32 s6, s6, 0x300
	v_bitop3_b32 v20, v1, s7, 15 bitop3:0x6c
	v_bitop3_b32 v25, v1, s8, 15 bitop3:0x6c
	s_or_b32 s8, s7, 6
	s_or_b32 s7, s7, 7
	v_cmp_eq_u32_e64 s[0:1], 0, v1
	v_and_b32_e32 v98, 0x70, v2
	v_bitop3_b32 v2, v2, s4, v3 bitop3:0x48
	v_and_b32_e32 v3, 32, v1
	v_ashrrev_i32_e32 v102, 3, v1
	v_ashrrev_i32_e32 v104, 3, v4
	v_ashrrev_i32_e32 v106, 3, v5
	v_ashrrev_i32_e32 v108, 3, v6
	v_ashrrev_i32_e32 v110, 3, v7
	v_ashrrev_i32_e32 v112, 3, v8
	v_ashrrev_i32_e32 v114, 3, v9
	v_ashrrev_i32_e32 v116, 3, v10
	v_ashrrev_i32_e32 v118, 3, v11
	v_ashrrev_i32_e32 v120, 3, v12
	v_ashrrev_i32_e32 v122, 3, v13
	v_ashrrev_i32_e32 v124, 3, v14
	v_ashrrev_i32_e32 v126, 3, v15
	v_ashrrev_i32_e32 v128, 3, v16
	v_ashrrev_i32_e32 v130, 3, v17
	v_ashrrev_i32_e32 v132, 3, v18
	v_or_b32_e32 v19, s6, v0
	v_bitop3_b32 v26, v1, s8, 15 bitop3:0x6c
	v_bitop3_b32 v1, v1, s7, 15 bitop3:0x6c
	v_mov_b32_e32 v97, 0
	v_cmp_eq_u32_e64 s[4:5], 0, v3
	v_lshlrev_b32_e32 v3, 7, v102
	v_lshlrev_b32_e32 v4, 7, v104
	v_lshlrev_b32_e32 v5, 7, v106
	v_lshlrev_b32_e32 v6, 7, v108
	v_lshlrev_b32_e32 v7, 7, v110
	v_lshlrev_b32_e32 v8, 7, v112
	v_lshlrev_b32_e32 v9, 7, v114
	v_lshlrev_b32_e32 v10, 7, v116
	v_lshlrev_b32_e32 v11, 7, v118
	v_lshlrev_b32_e32 v12, 7, v120
	v_lshlrev_b32_e32 v13, 7, v122
	v_lshlrev_b32_e32 v14, 7, v124
	v_lshlrev_b32_e32 v15, 7, v126
	v_lshlrev_b32_e32 v16, 7, v128
	v_lshlrev_b32_e32 v17, 7, v130
	v_lshlrev_b32_e32 v18, 7, v132
	v_lshl_add_u32 v20, v20, 3, 0
	v_lshlrev_b32_e32 v19, 7, v19
	v_lshl_add_u32 v21, v21, 3, 0
	v_lshl_add_u32 v22, v22, 3, 0
	v_lshl_add_u32 v23, v23, 3, 0
	v_lshl_add_u32 v24, v24, 3, 0
	v_lshl_add_u32 v25, v25, 3, 0
	v_lshl_add_u32 v26, v26, 3, 0
	v_lshl_add_u32 v1, v1, 3, 0
	v_add_u32_e32 v2, 0, v2
	s_mov_b32 s69, s60
	s_mov_b32 s9, 0
	v_mov_b32_e32 v99, v97
	v_and_b32_e32 v103, 0x7f, v102
	v_and_b32_e32 v105, 0x7f, v104
	v_and_b32_e32 v107, 0x7f, v106
	v_and_b32_e32 v109, 0x7f, v108
	v_and_b32_e32 v111, 0x7f, v110
	v_and_b32_e32 v113, 0x7f, v112
	v_and_b32_e32 v115, 0x7f, v114
	v_and_b32_e32 v117, 0x7f, v116
	v_and_b32_e32 v119, 0x7f, v118
	v_and_b32_e32 v121, 0x7f, v120
	v_and_b32_e32 v123, 0x7f, v122
	v_and_b32_e32 v125, 0x7f, v124
	v_and_b32_e32 v127, 0x7f, v126
	v_and_b32_e32 v129, 0x7f, v128
	v_and_b32_e32 v131, 0x7f, v130
	v_and_b32_e32 v133, 0x7f, v132
	s_add_i32 s17, 0, 0x20800
	s_lshl_b32 s18, s6, 2
	v_lshlrev_b32_e32 v96, 2, v0
	s_mov_b32 s19, 0x24000
	s_mov_b32 s20, 0x26000
	s_mov_b32 s21, 0x28000
	s_mov_b32 s22, 0x2a000
	s_mov_b32 s23, 0x2c000
	s_mov_b32 s24, 0x2e000
	v_add_u32_e32 v134, v20, v19
	s_mov_b32 s25, 0x30000
	s_mov_b32 s26, 0x32000
	s_mov_b32 s27, 0x34000
	s_mov_b32 s28, 0x36000
	s_mov_b32 s29, 0x38000
	s_mov_b32 s30, 0x3a000
	s_mov_b32 s31, 0x3c000
	s_mov_b32 s33, 0x3e000
	v_add_u32_e32 v135, v21, v19
	s_mov_b32 s34, 0x40000
	s_mov_b32 s35, 0x42000
	s_mov_b32 s36, 0x44000
	s_mov_b32 s37, 0x46000
	s_mov_b32 s38, 0x48000
	s_mov_b32 s39, 0x4a000
	s_mov_b32 s40, 0x4c000
	s_mov_b32 s41, 0x4e000
	v_add_u32_e32 v136, v22, v19
	s_mov_b32 s42, 0x50000
	s_mov_b32 s43, 0x52000
	s_mov_b32 s44, 0x54000
	s_mov_b32 s45, 0x56000
	s_mov_b32 s46, 0x58000
	s_mov_b32 s47, 0x5a000
	s_mov_b32 s48, 0x5c000
	s_mov_b32 s49, 0x5e000
	v_add_u32_e32 v137, v23, v19
	s_mov_b32 s50, 0x60000
	s_mov_b32 s51, 0x62000
	s_mov_b32 s52, 0x64000
	s_mov_b32 s53, 0x66000
	s_mov_b32 s54, 0x68000
	s_mov_b32 s55, 0x6a000
	s_mov_b32 s56, 0x6c000
	s_mov_b32 s57, 0x6e000
	v_add_u32_e32 v138, v24, v19
	s_mov_b32 s58, 0x70000
	s_mov_b32 s59, 0x72000
	s_mov_b32 s60, 0x74000
	s_mov_b32 s61, 0x76000
	s_mov_b32 s62, 0x78000
	s_mov_b32 s63, 0x7a000
	s_mov_b32 s64, 0x7c000
	s_mov_b32 s65, 0x7e000
	v_add_u32_e32 v139, v25, v19
	v_add_u32_e32 v140, v26, v19
	v_add_u32_e32 v141, v1, v19
	v_add_u32_e32 v142, v2, v3
	v_add_u32_e32 v143, v2, v4
	v_add_u32_e32 v144, v2, v5
	v_add_u32_e32 v145, v2, v6
	v_add_u32_e32 v146, v2, v7
	v_add_u32_e32 v147, v2, v8
	v_add_u32_e32 v148, v2, v9
	v_add_u32_e32 v149, v2, v10
	v_add_u32_e32 v150, v2, v11
	v_add_u32_e32 v151, v2, v12
	v_add_u32_e32 v152, v2, v13
	v_add_u32_e32 v153, v2, v14
	v_add_u32_e32 v154, v2, v15
	v_add_u32_e32 v155, v2, v16
	v_add_u32_e32 v156, v2, v17
	v_add_u32_e32 v157, v2, v18
	s_branch .LBB0_594

.LBB0_801:
	v_and_b32_e32 v5, 15, v4
	s_add_i32 s0, 0, 0x21000
	v_or_b32_e32 v6, s53, v5
	v_lshl_add_u32 v253, v4, 4, s0
	v_and_b32_e32 v7, 48, v4
	v_lshlrev_b32_e32 v8, 6, v6
	s_movk_i32 s0, 0x3c0
	v_and_or_b32 v8, v8, s0, v7
	v_lshlrev_b32_e32 v4, 2, v4
	s_add_u32 s0, s18, 0x80
	v_lshl_or_b32 v5, v5, 6, v7
	v_and_b32_e32 v4, 32, v4
	s_addc_u32 s1, s19, 0
	v_bitop3_b32 v158, v5, s56, v4 bitop3:0xde
	s_nop 0
	s_nop 0
	s_add_i32 m0, s7, 0x18000
	v_lshl_add_u64 v[4:5], s[0:1], 0, v[140:141]
	global_load_lds_dwordx4 v[4:5], off
	s_add_i32 m0, s7, 0x1a000
	v_lshl_add_u64 v[4:5], s[0:1], 0, v[142:143]
	s_add_u32 s0, s90, 0x12800080
	s_addc_u32 s1, s91, 0
	s_add_i32 s60, s7, 0x8000
	global_load_lds_dwordx4 v[4:5], off
	s_mov_b32 m0, s60
	v_lshl_add_u64 v[4:5], s[0:1], 0, v[0:1]
	s_add_i32 s61, s7, 0xa000
	global_load_lds_dwordx4 v[4:5], off
	v_lshl_add_u64 v[4:5], s[0:1], 0, v[144:145]
	s_add_u32 s0, s18, 0x40080
	s_mov_b32 m0, s61
	s_addc_u32 s1, s19, 0
	global_load_lds_dwordx4 v[4:5], off
	s_add_i32 m0, s7, 0x1c000
	v_lshl_add_u64 v[4:5], s[0:1], 0, v[140:141]
	global_load_lds_dwordx4 v[4:5], off
	v_lshl_add_u64 v[4:5], s[0:1], 0, v[142:143]
	s_add_i32 m0, s7, 0x1e000
	v_lshlrev_b32_e32 v6, 2, v6
	global_load_lds_dwordx4 v[4:5], off
	v_and_b32_e32 v6, 32, v6
	s_waitcnt vmcnt(8)
	s_barrier
	s_waitcnt vmcnt(6)
	v_readlane_b32 s0, v255, 25
	v_bitop3_b32 v6, v8, s55, v6 bitop3:0xde
	s_cmpk_lt_u32 s0, 0x100
	s_cselect_b64 s[22:23], -1, 0
	s_add_i32 s62, 0, 0x10000
	s_add_i32 s63, 0, 0x14000
	v_add_u32_e32 v143, 0, v6
	v_mov_b32_e32 v145, 0x7f7f7f7f
	s_mov_b32 s24, 0x3c800000
	s_mov_b32 s64, 0xc0c00000
	v_mov_b32_e32 v159, 0x41000000
	v_mov_b32_e32 v4, v141
	v_mov_b32_e32 v5, v141
	v_mov_b32_e32 v6, v141
	v_mov_b32_e32 v7, v141
	v_mov_b32_e32 v8, v141
	v_mov_b32_e32 v9, v141
	v_mov_b32_e32 v10, v141
	v_mov_b32_e32 v11, v141
	v_mov_b32_e32 v12, v141
	v_mov_b32_e32 v13, v141
	v_mov_b32_e32 v14, v141
	v_mov_b32_e32 v15, v141
	v_mov_b32_e32 v16, v141
	v_mov_b32_e32 v17, v141
	v_mov_b32_e32 v18, v141
	v_mov_b32_e32 v19, v141
	v_mov_b32_e32 v20, v141
	v_mov_b32_e32 v21, v141
	v_mov_b32_e32 v22, v141
	v_mov_b32_e32 v23, v141
	v_mov_b32_e32 v24, v141
	v_mov_b32_e32 v25, v141
	v_mov_b32_e32 v26, v141
	v_mov_b32_e32 v27, v141
	v_mov_b32_e32 v232, v141
	v_mov_b32_e32 v233, v141
	v_mov_b32_e32 v234, v141
	v_mov_b32_e32 v235, v141
	v_mov_b32_e32 v32, v141
	v_mov_b32_e32 v33, v141
	v_mov_b32_e32 v34, v141
	v_mov_b32_e32 v35, v141
	v_mov_b32_e32 v36, v141
	v_mov_b32_e32 v37, v141
	v_mov_b32_e32 v38, v141
	v_mov_b32_e32 v39, v141
	v_mov_b32_e32 v40, v141
	v_mov_b32_e32 v41, v141
	v_mov_b32_e32 v42, v141
	v_mov_b32_e32 v43, v141
	v_mov_b32_e32 v44, v141
	v_mov_b32_e32 v45, v141
	v_mov_b32_e32 v46, v141
	v_mov_b32_e32 v47, v141
	v_mov_b32_e32 v48, v141
	v_mov_b32_e32 v49, v141
	v_mov_b32_e32 v50, v141
	v_mov_b32_e32 v51, v141
	v_mov_b32_e32 v52, v141
	v_mov_b32_e32 v53, v141
	v_mov_b32_e32 v54, v141
	v_mov_b32_e32 v55, v141
	v_mov_b32_e32 v56, v141
	v_mov_b32_e32 v57, v141
	v_mov_b32_e32 v58, v141
	v_mov_b32_e32 v59, v141
	v_mov_b32_e32 v60, v141
	v_mov_b32_e32 v61, v141
	v_mov_b32_e32 v62, v141
	v_mov_b32_e32 v63, v141
	v_mov_b32_e32 v64, v141
	v_mov_b32_e32 v65, v141
	v_mov_b32_e32 v66, v141
	v_mov_b32_e32 v67, v141
	v_mov_b32_e32 v28, v141
	v_mov_b32_e32 v29, v141
	v_mov_b32_e32 v30, v141
	v_mov_b32_e32 v31, v141
	v_mov_b32_e32 v72, v141
	v_mov_b32_e32 v73, v141
	v_mov_b32_e32 v74, v141
	v_mov_b32_e32 v75, v141
	v_mov_b32_e32 v76, v141
	v_mov_b32_e32 v77, v141
	v_mov_b32_e32 v78, v141
	v_mov_b32_e32 v79, v141
	v_mov_b32_e32 v80, v141
	v_mov_b32_e32 v81, v141
	v_mov_b32_e32 v82, v141
	v_mov_b32_e32 v83, v141
	v_mov_b32_e32 v84, v141
	v_mov_b32_e32 v85, v141
	v_mov_b32_e32 v86, v141
	v_mov_b32_e32 v87, v141
	v_mov_b32_e32 v88, v141
	v_mov_b32_e32 v89, v141
	v_mov_b32_e32 v90, v141
	v_mov_b32_e32 v91, v141
	v_mov_b32_e32 v92, v141
	v_mov_b32_e32 v93, v141
	v_mov_b32_e32 v94, v141
	v_mov_b32_e32 v95, v141
	v_mov_b32_e32 v96, v141
	v_mov_b32_e32 v97, v141
	v_mov_b32_e32 v98, v141
	v_mov_b32_e32 v99, v141
	v_mov_b32_e32 v100, v141
	v_mov_b32_e32 v101, v141
	v_mov_b32_e32 v102, v141
	v_mov_b32_e32 v103, v141
	v_mov_b32_e32 v104, v141
	v_mov_b32_e32 v105, v141
	v_mov_b32_e32 v106, v141
	v_mov_b32_e32 v107, v141
	v_mov_b32_e32 v108, v141
	v_mov_b32_e32 v109, v141
	v_mov_b32_e32 v110, v141
	v_mov_b32_e32 v111, v141
	v_mov_b32_e32 v112, v141
	v_mov_b32_e32 v113, v141
	v_mov_b32_e32 v114, v141
	v_mov_b32_e32 v115, v141
	v_mov_b32_e32 v116, v141
	v_mov_b32_e32 v117, v141
	v_mov_b32_e32 v118, v141
	v_mov_b32_e32 v119, v141
	v_mov_b32_e32 v120, v141
	v_mov_b32_e32 v121, v141
	v_mov_b32_e32 v122, v141
	v_mov_b32_e32 v123, v141
	v_mov_b32_e32 v124, v141
	v_mov_b32_e32 v125, v141
	v_mov_b32_e32 v126, v141
	v_mov_b32_e32 v127, v141
	v_mov_b32_e32 v128, v141
	v_mov_b32_e32 v129, v141
	v_mov_b32_e32 v130, v141
	v_mov_b32_e32 v131, v141
	s_barrier
	s_branch .LBB0_804

.LBB0_886:
	v_and_b32_e32 v5, 15, v4
	s_add_i32 s0, 0, 0x21000
	v_or_b32_e32 v6, s53, v5
	v_lshl_add_u32 v253, v4, 4, s0
	v_and_b32_e32 v7, 48, v4
	v_lshlrev_b32_e32 v8, 6, v6
	s_movk_i32 s0, 0x3c0
	v_and_or_b32 v8, v8, s0, v7
	v_lshlrev_b32_e32 v4, 2, v4
	s_add_u32 s0, s18, 0x80
	v_lshl_or_b32 v5, v5, 6, v7
	v_and_b32_e32 v4, 32, v4
	s_addc_u32 s1, s19, 0
	v_bitop3_b32 v158, v5, s56, v4 bitop3:0xde
	s_nop 0
	s_nop 0
	s_add_i32 m0, s7, 0x18000
	v_lshl_add_u64 v[4:5], s[0:1], 0, v[140:141]
	v_lshlrev_b32_e32 v6, 2, v6
	global_load_lds_dwordx4 v[4:5], off
	s_add_i32 m0, s7, 0x1a000
	v_and_b32_e32 v6, 32, v6
	v_lshl_add_u64 v[4:5], s[0:1], 0, v[142:143]
	s_add_u32 s0, s90, 0x12800080
	v_bitop3_b32 v6, v8, s55, v6 bitop3:0xde
	s_addc_u32 s1, s91, 0
	s_add_i32 s55, s7, 0x8000
	global_load_lds_dwordx4 v[4:5], off
	s_mov_b32 m0, s55
	v_lshl_add_u64 v[4:5], s[0:1], 0, v[0:1]
	s_add_i32 s56, s7, 0xa000
	global_load_lds_dwordx4 v[4:5], off
	v_lshl_add_u64 v[4:5], s[0:1], 0, v[144:145]
	s_add_u32 s0, s18, 0x40080
	s_mov_b32 m0, s56
	s_addc_u32 s1, s19, 0
	global_load_lds_dwordx4 v[4:5], off
	s_add_i32 m0, s7, 0x1c000
	v_lshl_add_u64 v[4:5], s[0:1], 0, v[140:141]
	global_load_lds_dwordx4 v[4:5], off
	v_lshl_add_u64 v[4:5], s[0:1], 0, v[142:143]
	s_add_i32 m0, s7, 0x1e000
	v_readlane_b32 s0, v255, 25
	global_load_lds_dwordx4 v[4:5], off
	s_waitcnt vmcnt(8)
	s_barrier
	s_waitcnt vmcnt(6)
	s_cmpk_lt_u32 s0, 0x100
	s_cselect_b64 s[22:23], -1, 0
	s_add_i32 s57, 0, 0x10000
	s_add_i32 s61, 0, 0x14000
	v_add_u32_e32 v143, 0, v6
	v_mov_b32_e32 v145, 0x7f7f7f7f
	s_mov_b32 s24, 0x3c800000
	s_mov_b32 s62, 0xc0c00000
	s_mov_b32 s63, 0x40000
	v_mov_b32_e32 v159, 0x41000000
	v_mov_b32_e32 v4, v141
	v_mov_b32_e32 v5, v141
	v_mov_b32_e32 v6, v141
	v_mov_b32_e32 v7, v141
	v_mov_b32_e32 v8, v141
	v_mov_b32_e32 v9, v141
	v_mov_b32_e32 v10, v141
	v_mov_b32_e32 v11, v141
	v_mov_b32_e32 v12, v141
	v_mov_b32_e32 v13, v141
	v_mov_b32_e32 v14, v141
	v_mov_b32_e32 v15, v141
	v_mov_b32_e32 v16, v141
	v_mov_b32_e32 v17, v141
	v_mov_b32_e32 v18, v141
	v_mov_b32_e32 v19, v141
	v_mov_b32_e32 v20, v141
	v_mov_b32_e32 v21, v141
	v_mov_b32_e32 v22, v141
	v_mov_b32_e32 v23, v141
	v_mov_b32_e32 v24, v141
	v_mov_b32_e32 v25, v141
	v_mov_b32_e32 v26, v141
	v_mov_b32_e32 v27, v141
	v_mov_b32_e32 v232, v141
	v_mov_b32_e32 v233, v141
	v_mov_b32_e32 v234, v141
	v_mov_b32_e32 v235, v141
	v_mov_b32_e32 v32, v141
	v_mov_b32_e32 v33, v141
	v_mov_b32_e32 v34, v141
	v_mov_b32_e32 v35, v141
	v_mov_b32_e32 v36, v141
	v_mov_b32_e32 v37, v141
	v_mov_b32_e32 v38, v141
	v_mov_b32_e32 v39, v141
	v_mov_b32_e32 v40, v141
	v_mov_b32_e32 v41, v141
	v_mov_b32_e32 v42, v141
	v_mov_b32_e32 v43, v141
	v_mov_b32_e32 v44, v141
	v_mov_b32_e32 v45, v141
	v_mov_b32_e32 v46, v141
	v_mov_b32_e32 v47, v141
	v_mov_b32_e32 v48, v141
	v_mov_b32_e32 v49, v141
	v_mov_b32_e32 v50, v141
	v_mov_b32_e32 v51, v141
	v_mov_b32_e32 v52, v141
	v_mov_b32_e32 v53, v141
	v_mov_b32_e32 v54, v141
	v_mov_b32_e32 v55, v141
	v_mov_b32_e32 v56, v141
	v_mov_b32_e32 v57, v141
	v_mov_b32_e32 v58, v141
	v_mov_b32_e32 v59, v141
	v_mov_b32_e32 v60, v141
	v_mov_b32_e32 v61, v141
	v_mov_b32_e32 v62, v141
	v_mov_b32_e32 v63, v141
	v_mov_b32_e32 v64, v141
	v_mov_b32_e32 v65, v141
	v_mov_b32_e32 v66, v141
	v_mov_b32_e32 v67, v141
	v_mov_b32_e32 v28, v141
	v_mov_b32_e32 v29, v141
	v_mov_b32_e32 v30, v141
	v_mov_b32_e32 v31, v141
	v_mov_b32_e32 v72, v141
	v_mov_b32_e32 v73, v141
	v_mov_b32_e32 v74, v141
	v_mov_b32_e32 v75, v141
	v_mov_b32_e32 v76, v141
	v_mov_b32_e32 v77, v141
	v_mov_b32_e32 v78, v141
	v_mov_b32_e32 v79, v141
	v_mov_b32_e32 v80, v141
	v_mov_b32_e32 v81, v141
	v_mov_b32_e32 v82, v141
	v_mov_b32_e32 v83, v141
	v_mov_b32_e32 v84, v141
	v_mov_b32_e32 v85, v141
	v_mov_b32_e32 v86, v141
	v_mov_b32_e32 v87, v141
	v_mov_b32_e32 v88, v141
	v_mov_b32_e32 v89, v141
	v_mov_b32_e32 v90, v141
	v_mov_b32_e32 v91, v141
	v_mov_b32_e32 v92, v141
	v_mov_b32_e32 v93, v141
	v_mov_b32_e32 v94, v141
	v_mov_b32_e32 v95, v141
	v_mov_b32_e32 v96, v141
	v_mov_b32_e32 v97, v141
	v_mov_b32_e32 v98, v141
	v_mov_b32_e32 v99, v141
	v_mov_b32_e32 v100, v141
	v_mov_b32_e32 v101, v141
	v_mov_b32_e32 v102, v141
	v_mov_b32_e32 v103, v141
	v_mov_b32_e32 v104, v141
	v_mov_b32_e32 v105, v141
	v_mov_b32_e32 v106, v141
	v_mov_b32_e32 v107, v141
	v_mov_b32_e32 v108, v141
	v_mov_b32_e32 v109, v141
	v_mov_b32_e32 v110, v141
	v_mov_b32_e32 v111, v141
	v_mov_b32_e32 v112, v141
	v_mov_b32_e32 v113, v141
	v_mov_b32_e32 v114, v141
	v_mov_b32_e32 v115, v141
	v_mov_b32_e32 v116, v141
	v_mov_b32_e32 v117, v141
	v_mov_b32_e32 v118, v141
	v_mov_b32_e32 v119, v141
	v_mov_b32_e32 v120, v141
	v_mov_b32_e32 v121, v141
	v_mov_b32_e32 v122, v141
	v_mov_b32_e32 v123, v141
	v_mov_b32_e32 v124, v141
	v_mov_b32_e32 v125, v141
	v_mov_b32_e32 v126, v141
	v_mov_b32_e32 v127, v141
	v_mov_b32_e32 v128, v141
	v_mov_b32_e32 v129, v141
	v_mov_b32_e32 v130, v141
	v_mov_b32_e32 v131, v141
	s_barrier
	s_branch .LBB0_889

.LBB0_1031:
	s_add_i32 s16, 0, 0x21000
	v_lshl_add_u32 v252, v4, 4, s16
	s_add_u32 s16, s90, 0x1e800000
	v_and_b32_e32 v5, 48, v4
	v_lshlrev_b32_e32 v6, 6, v4
	s_movk_i32 s19, 0x3c0
	v_lshlrev_b32_e32 v4, 2, v4
	s_addc_u32 s17, s91, 0
	s_lshl_b32 s53, s18, 6
	s_lshl_b32 s18, s18, 13
	v_and_or_b32 v5, v6, s19, v5
	v_and_b32_e32 v4, 32, v4
	v_bitop3_b32 v6, v5, s18, v4 bitop3:0xde
	s_lshl_b32 s18, s94, 5
	s_and_b32 s55, s18, 0x60
	s_lshl_b32 s18, s55, 7
	v_bitop3_b32 v158, v5, s18, v4 bitop3:0xde
	s_add_u32 s18, s12, 0x80
	s_addc_u32 s19, s13, 0
	s_nop 0
	s_nop 0
	s_add_i32 m0, s1, 0x18000
	v_lshl_add_u64 v[4:5], s[18:19], 0, v[148:149]
	global_load_lds_dwordx4 v[4:5], off
	s_add_i32 m0, s1, 0x1a000
	v_lshl_add_u64 v[4:5], s[18:19], 0, v[150:151]
	s_add_u32 s18, s90, 0x14800080
	s_addc_u32 s19, s91, 0
	s_add_i32 s56, s1, 0x8000
	global_load_lds_dwordx4 v[4:5], off
	s_mov_b32 m0, s56
	v_lshl_add_u64 v[4:5], s[18:19], 0, v[0:1]
	s_add_i32 s57, s1, 0xa000
	global_load_lds_dwordx4 v[4:5], off
	v_lshl_add_u64 v[4:5], s[18:19], 0, v[152:153]
	s_add_u32 s18, s12, 0x40080
	s_mov_b32 m0, s57
	s_addc_u32 s19, s13, 0
	global_load_lds_dwordx4 v[4:5], off
	s_add_i32 m0, s1, 0x1c000
	v_lshl_add_u64 v[4:5], s[18:19], 0, v[148:149]
	global_load_lds_dwordx4 v[4:5], off
	v_lshl_add_u64 v[4:5], s[18:19], 0, v[150:151]
	s_add_i32 m0, s1, 0x1e000
	v_readlane_b32 s18, v255, 25
	global_load_lds_dwordx4 v[4:5], off
	s_waitcnt vmcnt(8)
	s_barrier
	s_waitcnt vmcnt(6)
	s_cmpk_lt_u32 s18, 0x100
	s_cselect_b64 s[18:19], -1, 0
	s_add_i32 s58, 0, 0x10000
	s_add_i32 s59, 0, 0x14000
	v_add_u32_e32 v151, 0, v6
	v_mov_b32_e32 v153, 0x7f7f7f7f
	s_mov_b32 s20, 0x3c800000
	s_mov_b32 s60, 0x40000
	s_mov_b32 s61, 0x50000
	s_mov_b32 s22, s0
	v_mov_b32_e32 v4, v149
	v_mov_b32_e32 v5, v149
	v_mov_b32_e32 v6, v149
	v_mov_b32_e32 v7, v149
	v_mov_b32_e32 v8, v149
	v_mov_b32_e32 v9, v149
	v_mov_b32_e32 v10, v149
	v_mov_b32_e32 v11, v149
	v_mov_b32_e32 v12, v149
	v_mov_b32_e32 v13, v149
	v_mov_b32_e32 v14, v149
	v_mov_b32_e32 v15, v149
	v_mov_b32_e32 v16, v149
	v_mov_b32_e32 v17, v149
	v_mov_b32_e32 v18, v149
	v_mov_b32_e32 v19, v149
	v_mov_b32_e32 v20, v149
	v_mov_b32_e32 v21, v149
	v_mov_b32_e32 v22, v149
	v_mov_b32_e32 v23, v149
	v_mov_b32_e32 v24, v149
	v_mov_b32_e32 v25, v149
	v_mov_b32_e32 v26, v149
	v_mov_b32_e32 v27, v149
	v_mov_b32_e32 v232, v149
	v_mov_b32_e32 v233, v149
	v_mov_b32_e32 v234, v149
	v_mov_b32_e32 v235, v149
	v_mov_b32_e32 v32, v149
	v_mov_b32_e32 v33, v149
	v_mov_b32_e32 v34, v149
	v_mov_b32_e32 v35, v149
	v_mov_b32_e32 v36, v149
	v_mov_b32_e32 v37, v149
	v_mov_b32_e32 v38, v149
	v_mov_b32_e32 v39, v149
	v_mov_b32_e32 v40, v149
	v_mov_b32_e32 v41, v149
	v_mov_b32_e32 v42, v149
	v_mov_b32_e32 v43, v149
	v_mov_b32_e32 v44, v149
	v_mov_b32_e32 v45, v149
	v_mov_b32_e32 v46, v149
	v_mov_b32_e32 v47, v149
	v_mov_b32_e32 v48, v149
	v_mov_b32_e32 v49, v149
	v_mov_b32_e32 v50, v149
	v_mov_b32_e32 v51, v149
	v_mov_b32_e32 v52, v149
	v_mov_b32_e32 v53, v149
	v_mov_b32_e32 v54, v149
	v_mov_b32_e32 v55, v149
	v_mov_b32_e32 v56, v149
	v_mov_b32_e32 v57, v149
	v_mov_b32_e32 v58, v149
	v_mov_b32_e32 v59, v149
	v_mov_b32_e32 v60, v149
	v_mov_b32_e32 v61, v149
	v_mov_b32_e32 v62, v149
	v_mov_b32_e32 v63, v149
	v_mov_b32_e32 v64, v149
	v_mov_b32_e32 v65, v149
	v_mov_b32_e32 v66, v149
	v_mov_b32_e32 v67, v149
	v_mov_b32_e32 v28, v149
	v_mov_b32_e32 v29, v149
	v_mov_b32_e32 v30, v149
	v_mov_b32_e32 v31, v149
	v_mov_b32_e32 v72, v149
	v_mov_b32_e32 v73, v149
	v_mov_b32_e32 v74, v149
	v_mov_b32_e32 v75, v149
	v_mov_b32_e32 v76, v149
	v_mov_b32_e32 v77, v149
	v_mov_b32_e32 v78, v149
	v_mov_b32_e32 v79, v149
	v_mov_b32_e32 v80, v149
	v_mov_b32_e32 v81, v149
	v_mov_b32_e32 v82, v149
	v_mov_b32_e32 v83, v149
	v_mov_b32_e32 v84, v149
	v_mov_b32_e32 v85, v149
	v_mov_b32_e32 v86, v149
	v_mov_b32_e32 v87, v149
	v_mov_b32_e32 v88, v149
	v_mov_b32_e32 v89, v149
	v_mov_b32_e32 v90, v149
	v_mov_b32_e32 v91, v149
	v_mov_b32_e32 v92, v149
	v_mov_b32_e32 v93, v149
	v_mov_b32_e32 v94, v149
	v_mov_b32_e32 v95, v149
	v_mov_b32_e32 v96, v149
	v_mov_b32_e32 v97, v149
	v_mov_b32_e32 v98, v149
	v_mov_b32_e32 v99, v149
	v_mov_b32_e32 v100, v149
	v_mov_b32_e32 v101, v149
	v_mov_b32_e32 v102, v149
	v_mov_b32_e32 v103, v149
	v_mov_b32_e32 v104, v149
	v_mov_b32_e32 v105, v149
	v_mov_b32_e32 v106, v149
	v_mov_b32_e32 v107, v149
	v_mov_b32_e32 v108, v149
	v_mov_b32_e32 v109, v149
	v_mov_b32_e32 v110, v149
	v_mov_b32_e32 v111, v149
	v_mov_b32_e32 v112, v149
	v_mov_b32_e32 v113, v149
	v_mov_b32_e32 v114, v149
	v_mov_b32_e32 v115, v149
	v_mov_b32_e32 v116, v149
	v_mov_b32_e32 v117, v149
	v_mov_b32_e32 v118, v149
	v_mov_b32_e32 v119, v149
	v_mov_b32_e32 v120, v149
	v_mov_b32_e32 v121, v149
	v_mov_b32_e32 v122, v149
	v_mov_b32_e32 v123, v149
	v_mov_b32_e32 v124, v149
	v_mov_b32_e32 v125, v149
	v_mov_b32_e32 v126, v149
	v_mov_b32_e32 v127, v149
	v_mov_b32_e32 v128, v149
	v_mov_b32_e32 v129, v149
	v_mov_b32_e32 v130, v149
	v_mov_b32_e32 v131, v149
	s_barrier
	s_branch .LBB0_1034
